# speedup vs baseline: 1.0699x; 1.0185x over previous
.LBB2_10:
	s_or_b64 exec, exec, s[10:11]
	v_mov_b32_e32 v52, 0x7bff7bff
	v_mov_b32_e32 v99, 0x7bff7bff
	v_mov_b32_e32 v98, 0x7bff7bff
	v_mov_b32_e32 v103, 0x7bff7bff
	v_mov_b32_e32 v100, 0xfbfffbff
	v_mov_b32_e32 v101, 0xfbfffbff
	v_mov_b32_e32 v105, 0xfbfffbff
	v_mov_b32_e32 v104, 0xfbfffbff
	v_mov_b64_e32 v[62:63], 0
	v_mov_b64_e32 v[64:65], 0
	v_mov_b64_e32 v[66:67], 0
	v_mov_b64_e32 v[68:69], 0
	v_mov_b64_e32 v[70:71], 0
	v_mov_b64_e32 v[72:73], 0
	v_mov_b64_e32 v[74:75], 0
	v_mov_b64_e32 v[76:77], 0
	v_cmp_lt_i32_e64 s[10:11], v50, v97
	v_mov_b32_e32 v91, v97
	v_and_b32_e32 v92, 3, v50
	s_waitcnt lgkmcnt(0)
	v_cndmask_b32_e64 v10, v11, v10, s[10:11]
	v_add_u32_e32 v92, 8, v92
	v_add_u32_e32 v93, -1, v97
	v_cndmask_b32_e64 v81, 0, v10, s[0:1]
	v_cndmask_b32_e64 v93, 0, v93, s[0:1]
	v_cndmask_b32_e64 v94, 0, v78, s[0:1]
	v_lshlrev_b32_e32 v81, 7, v81
	v_min_i32_e32 v116, v92, v93
	v_add_u32_e32 v117, 4, v92
	v_min_i32_e32 v117, v117, v93
	v_add_lshl_u32 v116, v116, v94, 2
	v_add_lshl_u32 v117, v117, v94, 2
	global_load_dword v87, v116, s[24:25]
	global_load_dword v88, v117, s[24:25]
	v_add_u32_e32 v92, 8, v92
	v_mov_b32_e32 v89, v81
	v_mov_b32_e32 v90, v81
	s_nop 1
	v_mov_b32_dpp v89, v81 row_shr:4 row_mask:0xf bank_mask:0xa
	v_mov_b32_dpp v90, v81 row_shl:4 row_mask:0xf bank_mask:0x5
	s_mov_b64 s[78:79], 0xff
	v_cmp_gt_i32_e64 s[44:45], v91, 0
	v_cmp_gt_i32_e64 s[46:47], v91, 1
	v_cmp_gt_i32_e64 s[48:49], v91, 2
	v_cmp_gt_i32_e64 s[50:51], v91, 3
	v_cmp_gt_i32_e64 s[52:53], v91, 4
	v_cmp_gt_i32_e64 s[54:55], v91, 5
	v_cmp_gt_i32_e64 s[56:57], v91, 6
	v_cmp_gt_i32_e64 s[58:59], v91, 7
	s_nop 0
	v_or_b32_dpp v79, v89, v56 quad_perm:[0,0,0,0] row_mask:0xf bank_mask:0xf
	v_or_b32_dpp v80, v89, v56 quad_perm:[1,1,1,1] row_mask:0xf bank_mask:0xf
	s_or_b64 exec, s[44:45], s[78:79]
	global_load_dwordx4 v[10:13], v79, s[30:31]
	global_load_dwordx4 v[14:17], v80, s[30:31]
	s_mov_b64 exec, -1
	s_nop 0
	v_or_b32_dpp v79, v89, v56 quad_perm:[2,2,2,2] row_mask:0xf bank_mask:0xf
	v_or_b32_dpp v80, v89, v56 quad_perm:[3,3,3,3] row_mask:0xf bank_mask:0xf
	s_or_b64 exec, s[48:49], s[78:79]
	global_load_dwordx4 v[18:21], v79, s[30:31]
	global_load_dwordx4 v[22:25], v80, s[30:31]
	s_mov_b64 exec, -1
	s_nop 0
	v_or_b32_dpp v79, v90, v56 quad_perm:[0,0,0,0] row_mask:0xf bank_mask:0xf
	v_or_b32_dpp v80, v90, v56 quad_perm:[1,1,1,1] row_mask:0xf bank_mask:0xf
	s_or_b64 exec, s[52:53], s[78:79]
	global_load_dwordx4 v[26:29], v79, s[30:31]
	global_load_dwordx4 v[30:33], v80, s[30:31]
	s_mov_b64 exec, -1
	s_nop 0
	v_or_b32_dpp v79, v90, v56 quad_perm:[2,2,2,2] row_mask:0xf bank_mask:0xf
	v_or_b32_dpp v80, v90, v56 quad_perm:[3,3,3,3] row_mask:0xf bank_mask:0xf
	s_or_b64 exec, s[56:57], s[78:79]
	global_load_dwordx4 v[34:37], v79, s[30:31]
	global_load_dwordx4 v[38:41], v80, s[30:31]
	s_mov_b64 exec, -1
	v_cmp_gt_i32_e64 s[60:61], v91, 8
	s_cmp_lg_u64 s[60:61], 0
	s_cbranch_scc0 .Lpl_last_a0
.Lpl_steady_a0:
	s_waitcnt vmcnt(6)
	v_lshlrev_b32_e32 v89, 7, v87
	v_lshlrev_b32_e32 v90, 7, v88
	v_min_i32_e32 v116, v92, v93
	v_add_u32_e32 v117, 4, v92
	v_min_i32_e32 v117, v117, v93
	v_add_lshl_u32 v116, v116, v94, 2
	v_add_lshl_u32 v117, v117, v94, 2
	global_load_dword v87, v116, s[24:25]
	global_load_dword v88, v117, s[24:25]
	v_add_u32_e32 v92, 8, v92
	v_cmp_gt_i32_e64 s[62:63], v91, 8
	v_cmp_gt_i32_e64 s[64:65], v91, 9
	v_cmp_gt_i32_e64 s[66:67], v91, 10
	v_cmp_gt_i32_e64 s[68:69], v91, 11
	v_cmp_gt_i32_e64 s[70:71], v91, 12
	v_cmp_gt_i32_e64 s[72:73], v91, 13
	v_cmp_gt_i32_e64 s[74:75], v91, 14
	v_cmp_gt_i32_e64 s[76:77], v91, 15
	s_mov_b64 exec, s[44:45]
	v_pk_minimum3_f16 v52, v52, v10, v14
	v_pk_maximum3_f16 v100, v100, v10, v14
	v_pk_minimum3_f16 v99, v99, v11, v15
	v_pk_maximum3_f16 v101, v101, v11, v15
	v_pk_minimum3_f16 v98, v98, v12, v16
	v_pk_maximum3_f16 v105, v105, v12, v16
	v_pk_minimum3_f16 v103, v103, v13, v17
	v_pk_maximum3_f16 v104, v104, v13, v17
	v_pk_mul_f16 v110, v10, v10
	v_mov_b32_e32 v106, v10
	v_pk_mul_f16 v111, v11, v11
	v_mov_b32_e32 v107, v11
	v_pk_mul_f16 v112, v12, v12
	v_mov_b32_e32 v108, v12
	v_pk_mul_f16 v113, v13, v13
	v_mov_b32_e32 v109, v13
	s_mov_b64 exec, s[46:47]
	v_pk_add_f16 v106, v106, v14
	v_pk_fma_f16 v110, v14, v14, v110
	v_pk_add_f16 v107, v107, v15
	v_pk_fma_f16 v111, v15, v15, v111
	v_pk_add_f16 v108, v108, v16
	v_pk_fma_f16 v112, v16, v16, v112
	v_pk_add_f16 v109, v109, v17
	v_pk_fma_f16 v113, v17, v17, v113
	s_mov_b64 exec, -1
	s_nop 0
	v_or_b32_dpp v79, v89, v56 quad_perm:[0,0,0,0] row_mask:0xf bank_mask:0xf
	v_or_b32_dpp v80, v89, v56 quad_perm:[1,1,1,1] row_mask:0xf bank_mask:0xf
	s_or_b64 exec, s[62:63], s[78:79]
	global_load_dwordx4 v[10:13], v79, s[30:31]
	global_load_dwordx4 v[14:17], v80, s[30:31]
	s_mov_b64 exec, -1
	s_waitcnt vmcnt(8)
	s_mov_b64 exec, s[48:49]
	v_pk_minimum3_f16 v52, v52, v18, v22
	v_pk_maximum3_f16 v100, v100, v18, v22
	v_pk_minimum3_f16 v99, v99, v19, v23
	v_pk_maximum3_f16 v101, v101, v19, v23
	v_pk_minimum3_f16 v98, v98, v20, v24
	v_pk_maximum3_f16 v105, v105, v20, v24
	v_pk_minimum3_f16 v103, v103, v21, v25
	v_pk_maximum3_f16 v104, v104, v21, v25
	v_pk_add_f16 v106, v106, v18
	v_pk_fma_f16 v110, v18, v18, v110
	v_pk_add_f16 v107, v107, v19
	v_pk_fma_f16 v111, v19, v19, v111
	v_pk_add_f16 v108, v108, v20
	v_pk_fma_f16 v112, v20, v20, v112
	v_pk_add_f16 v109, v109, v21
	v_pk_fma_f16 v113, v21, v21, v113
	s_mov_b64 exec, s[50:51]
	v_pk_add_f16 v106, v106, v22
	v_pk_fma_f16 v110, v22, v22, v110
	v_pk_add_f16 v107, v107, v23
	v_pk_fma_f16 v111, v23, v23, v111
	v_pk_add_f16 v108, v108, v24
	v_pk_fma_f16 v112, v24, v24, v112
	v_pk_add_f16 v109, v109, v25
	v_pk_fma_f16 v113, v25, v25, v113
	s_mov_b64 exec, -1
	s_nop 0
	v_or_b32_dpp v79, v89, v56 quad_perm:[2,2,2,2] row_mask:0xf bank_mask:0xf
	v_or_b32_dpp v80, v89, v56 quad_perm:[3,3,3,3] row_mask:0xf bank_mask:0xf
	s_or_b64 exec, s[66:67], s[78:79]
	global_load_dwordx4 v[18:21], v79, s[30:31]
	global_load_dwordx4 v[22:25], v80, s[30:31]
	s_mov_b64 exec, -1
	s_waitcnt vmcnt(8)
	s_mov_b64 exec, s[52:53]
	v_pk_minimum3_f16 v52, v52, v26, v30
	v_pk_maximum3_f16 v100, v100, v26, v30
	v_pk_minimum3_f16 v99, v99, v27, v31
	v_pk_maximum3_f16 v101, v101, v27, v31
	v_pk_minimum3_f16 v98, v98, v28, v32
	v_pk_maximum3_f16 v105, v105, v28, v32
	v_pk_minimum3_f16 v103, v103, v29, v33
	v_pk_maximum3_f16 v104, v104, v29, v33
	v_pk_add_f16 v106, v106, v26
	v_pk_fma_f16 v110, v26, v26, v110
	v_pk_add_f16 v107, v107, v27
	v_pk_fma_f16 v111, v27, v27, v111
	v_pk_add_f16 v108, v108, v28
	v_pk_fma_f16 v112, v28, v28, v112
	v_pk_add_f16 v109, v109, v29
	v_pk_fma_f16 v113, v29, v29, v113
	s_mov_b64 exec, s[54:55]
	v_pk_add_f16 v106, v106, v30
	v_pk_fma_f16 v110, v30, v30, v110
	v_pk_add_f16 v107, v107, v31
	v_pk_fma_f16 v111, v31, v31, v111
	v_pk_add_f16 v108, v108, v32
	v_pk_fma_f16 v112, v32, v32, v112
	v_pk_add_f16 v109, v109, v33
	v_pk_fma_f16 v113, v33, v33, v113
	s_mov_b64 exec, -1
	s_nop 0
	v_or_b32_dpp v79, v90, v56 quad_perm:[0,0,0,0] row_mask:0xf bank_mask:0xf
	v_or_b32_dpp v80, v90, v56 quad_perm:[1,1,1,1] row_mask:0xf bank_mask:0xf
	s_or_b64 exec, s[70:71], s[78:79]
	global_load_dwordx4 v[26:29], v79, s[30:31]
	global_load_dwordx4 v[30:33], v80, s[30:31]
	s_mov_b64 exec, -1
	s_waitcnt vmcnt(8)
	s_mov_b64 exec, s[56:57]
	v_pk_minimum3_f16 v52, v52, v34, v38
	v_pk_maximum3_f16 v100, v100, v34, v38
	v_pk_minimum3_f16 v99, v99, v35, v39
	v_pk_maximum3_f16 v101, v101, v35, v39
	v_pk_minimum3_f16 v98, v98, v36, v40
	v_pk_maximum3_f16 v105, v105, v36, v40
	v_pk_minimum3_f16 v103, v103, v37, v41
	v_pk_maximum3_f16 v104, v104, v37, v41
	v_pk_add_f16 v106, v106, v34
	v_pk_fma_f16 v110, v34, v34, v110
	v_pk_add_f16 v107, v107, v35
	v_pk_fma_f16 v111, v35, v35, v111
	v_pk_add_f16 v108, v108, v36
	v_pk_fma_f16 v112, v36, v36, v112
	v_pk_add_f16 v109, v109, v37
	v_pk_fma_f16 v113, v37, v37, v113
	s_mov_b64 exec, s[58:59]
	v_pk_add_f16 v106, v106, v38
	v_pk_fma_f16 v110, v38, v38, v110
	v_pk_add_f16 v107, v107, v39
	v_pk_fma_f16 v111, v39, v39, v111
	v_pk_add_f16 v108, v108, v40
	v_pk_fma_f16 v112, v40, v40, v112
	v_pk_add_f16 v109, v109, v41
	v_pk_fma_f16 v113, v41, v41, v113
	s_mov_b64 exec, -1
	s_nop 0
	v_or_b32_dpp v79, v90, v56 quad_perm:[2,2,2,2] row_mask:0xf bank_mask:0xf
	v_or_b32_dpp v80, v90, v56 quad_perm:[3,3,3,3] row_mask:0xf bank_mask:0xf
	s_or_b64 exec, s[74:75], s[78:79]
	global_load_dwordx4 v[34:37], v79, s[30:31]
	global_load_dwordx4 v[38:41], v80, s[30:31]
	s_mov_b64 exec, -1
	s_mov_b64 exec, s[44:45]
	v_fma_mix_f32 v72, v106, 1.0, v72 op_sel_hi:[1,0,0]
	v_fma_mix_f32 v73, v106, 1.0, v73 op_sel:[1,0,0] op_sel_hi:[1,0,0]
	v_fma_mix_f32 v76, v110, 1.0, v76 op_sel_hi:[1,0,0]
	v_fma_mix_f32 v77, v110, 1.0, v77 op_sel:[1,0,0] op_sel_hi:[1,0,0]
	v_fma_mix_f32 v70, v107, 1.0, v70 op_sel_hi:[1,0,0]
	v_fma_mix_f32 v71, v107, 1.0, v71 op_sel:[1,0,0] op_sel_hi:[1,0,0]
	v_fma_mix_f32 v74, v111, 1.0, v74 op_sel_hi:[1,0,0]
	v_fma_mix_f32 v75, v111, 1.0, v75 op_sel:[1,0,0] op_sel_hi:[1,0,0]
	v_fma_mix_f32 v64, v108, 1.0, v64 op_sel_hi:[1,0,0]
	v_fma_mix_f32 v65, v108, 1.0, v65 op_sel:[1,0,0] op_sel_hi:[1,0,0]
	v_fma_mix_f32 v68, v112, 1.0, v68 op_sel_hi:[1,0,0]
	v_fma_mix_f32 v69, v112, 1.0, v69 op_sel:[1,0,0] op_sel_hi:[1,0,0]
	v_fma_mix_f32 v62, v109, 1.0, v62 op_sel_hi:[1,0,0]
	v_fma_mix_f32 v63, v109, 1.0, v63 op_sel:[1,0,0] op_sel_hi:[1,0,0]
	v_fma_mix_f32 v66, v113, 1.0, v66 op_sel_hi:[1,0,0]
	v_fma_mix_f32 v67, v113, 1.0, v67 op_sel:[1,0,0] op_sel_hi:[1,0,0]
	s_mov_b64 exec, -1
	s_mov_b64 s[44:45], s[62:63]
	s_mov_b64 s[46:47], s[64:65]
	s_mov_b64 s[48:49], s[66:67]
	s_mov_b64 s[50:51], s[68:69]
	s_mov_b64 s[52:53], s[70:71]
	s_mov_b64 s[54:55], s[72:73]
	s_mov_b64 s[56:57], s[74:75]
	s_mov_b64 s[58:59], s[76:77]
	v_add_u32_e32 v91, -8, v91
	v_cmp_gt_i32_e64 s[60:61], v91, 8
	s_cmp_lg_u64 s[60:61], 0
	s_cbranch_scc1 .Lpl_steady_a0
.Lpl_last_a0:
	s_waitcnt vmcnt(6)
	s_mov_b64 exec, s[44:45]
	v_pk_minimum3_f16 v52, v52, v10, v14
	v_pk_maximum3_f16 v100, v100, v10, v14
	v_pk_minimum3_f16 v99, v99, v11, v15
	v_pk_maximum3_f16 v101, v101, v11, v15
	v_pk_minimum3_f16 v98, v98, v12, v16
	v_pk_maximum3_f16 v105, v105, v12, v16
	v_pk_minimum3_f16 v103, v103, v13, v17
	v_pk_maximum3_f16 v104, v104, v13, v17
	v_pk_mul_f16 v110, v10, v10
	v_mov_b32_e32 v106, v10
	v_pk_mul_f16 v111, v11, v11
	v_mov_b32_e32 v107, v11
	v_pk_mul_f16 v112, v12, v12
	v_mov_b32_e32 v108, v12
	v_pk_mul_f16 v113, v13, v13
	v_mov_b32_e32 v109, v13
	s_mov_b64 exec, s[46:47]
	v_pk_add_f16 v106, v106, v14
	v_pk_fma_f16 v110, v14, v14, v110
	v_pk_add_f16 v107, v107, v15
	v_pk_fma_f16 v111, v15, v15, v111
	v_pk_add_f16 v108, v108, v16
	v_pk_fma_f16 v112, v16, v16, v112
	v_pk_add_f16 v109, v109, v17
	v_pk_fma_f16 v113, v17, v17, v113
	s_mov_b64 exec, -1
	s_cmp_eq_u64 s[48:49], 0
	s_cbranch_scc1 .Lpl_fold_a0
	s_waitcnt vmcnt(4)
	s_mov_b64 exec, s[48:49]
	v_pk_minimum3_f16 v52, v52, v18, v22
	v_pk_maximum3_f16 v100, v100, v18, v22
	v_pk_minimum3_f16 v99, v99, v19, v23
	v_pk_maximum3_f16 v101, v101, v19, v23
	v_pk_minimum3_f16 v98, v98, v20, v24
	v_pk_maximum3_f16 v105, v105, v20, v24
	v_pk_minimum3_f16 v103, v103, v21, v25
	v_pk_maximum3_f16 v104, v104, v21, v25
	v_pk_add_f16 v106, v106, v18
	v_pk_fma_f16 v110, v18, v18, v110
	v_pk_add_f16 v107, v107, v19
	v_pk_fma_f16 v111, v19, v19, v111
	v_pk_add_f16 v108, v108, v20
	v_pk_fma_f16 v112, v20, v20, v112
	v_pk_add_f16 v109, v109, v21
	v_pk_fma_f16 v113, v21, v21, v113
	s_mov_b64 exec, s[50:51]
	v_pk_add_f16 v106, v106, v22
	v_pk_fma_f16 v110, v22, v22, v110
	v_pk_add_f16 v107, v107, v23
	v_pk_fma_f16 v111, v23, v23, v111
	v_pk_add_f16 v108, v108, v24
	v_pk_fma_f16 v112, v24, v24, v112
	v_pk_add_f16 v109, v109, v25
	v_pk_fma_f16 v113, v25, v25, v113
	s_mov_b64 exec, -1
	s_cmp_eq_u64 s[52:53], 0
	s_cbranch_scc1 .Lpl_fold_a0
	s_waitcnt vmcnt(2)
	s_mov_b64 exec, s[52:53]
	v_pk_minimum3_f16 v52, v52, v26, v30
	v_pk_maximum3_f16 v100, v100, v26, v30
	v_pk_minimum3_f16 v99, v99, v27, v31
	v_pk_maximum3_f16 v101, v101, v27, v31
	v_pk_minimum3_f16 v98, v98, v28, v32
	v_pk_maximum3_f16 v105, v105, v28, v32
	v_pk_minimum3_f16 v103, v103, v29, v33
	v_pk_maximum3_f16 v104, v104, v29, v33
	v_pk_add_f16 v106, v106, v26
	v_pk_fma_f16 v110, v26, v26, v110
	v_pk_add_f16 v107, v107, v27
	v_pk_fma_f16 v111, v27, v27, v111
	v_pk_add_f16 v108, v108, v28
	v_pk_fma_f16 v112, v28, v28, v112
	v_pk_add_f16 v109, v109, v29
	v_pk_fma_f16 v113, v29, v29, v113
	s_mov_b64 exec, s[54:55]
	v_pk_add_f16 v106, v106, v30
	v_pk_fma_f16 v110, v30, v30, v110
	v_pk_add_f16 v107, v107, v31
	v_pk_fma_f16 v111, v31, v31, v111
	v_pk_add_f16 v108, v108, v32
	v_pk_fma_f16 v112, v32, v32, v112
	v_pk_add_f16 v109, v109, v33
	v_pk_fma_f16 v113, v33, v33, v113
	s_mov_b64 exec, -1
	s_cmp_eq_u64 s[56:57], 0
	s_cbranch_scc1 .Lpl_fold_a0
	s_waitcnt vmcnt(0)
	s_mov_b64 exec, s[56:57]
	v_pk_minimum3_f16 v52, v52, v34, v38
	v_pk_maximum3_f16 v100, v100, v34, v38
	v_pk_minimum3_f16 v99, v99, v35, v39
	v_pk_maximum3_f16 v101, v101, v35, v39
	v_pk_minimum3_f16 v98, v98, v36, v40
	v_pk_maximum3_f16 v105, v105, v36, v40
	v_pk_minimum3_f16 v103, v103, v37, v41
	v_pk_maximum3_f16 v104, v104, v37, v41
	v_pk_add_f16 v106, v106, v34
	v_pk_fma_f16 v110, v34, v34, v110
	v_pk_add_f16 v107, v107, v35
	v_pk_fma_f16 v111, v35, v35, v111
	v_pk_add_f16 v108, v108, v36
	v_pk_fma_f16 v112, v36, v36, v112
	v_pk_add_f16 v109, v109, v37
	v_pk_fma_f16 v113, v37, v37, v113
	s_mov_b64 exec, s[58:59]
	v_pk_add_f16 v106, v106, v38
	v_pk_fma_f16 v110, v38, v38, v110
	v_pk_add_f16 v107, v107, v39
	v_pk_fma_f16 v111, v39, v39, v111
	v_pk_add_f16 v108, v108, v40
	v_pk_fma_f16 v112, v40, v40, v112
	v_pk_add_f16 v109, v109, v41
	v_pk_fma_f16 v113, v41, v41, v113
	s_mov_b64 exec, -1
.Lpl_fold_a0:
	s_mov_b64 exec, s[44:45]
	v_fma_mix_f32 v72, v106, 1.0, v72 op_sel_hi:[1,0,0]
	v_fma_mix_f32 v73, v106, 1.0, v73 op_sel:[1,0,0] op_sel_hi:[1,0,0]
	v_fma_mix_f32 v76, v110, 1.0, v76 op_sel_hi:[1,0,0]
	v_fma_mix_f32 v77, v110, 1.0, v77 op_sel:[1,0,0] op_sel_hi:[1,0,0]
	v_fma_mix_f32 v70, v107, 1.0, v70 op_sel_hi:[1,0,0]
	v_fma_mix_f32 v71, v107, 1.0, v71 op_sel:[1,0,0] op_sel_hi:[1,0,0]
	v_fma_mix_f32 v74, v111, 1.0, v74 op_sel_hi:[1,0,0]
	v_fma_mix_f32 v75, v111, 1.0, v75 op_sel:[1,0,0] op_sel_hi:[1,0,0]
	v_fma_mix_f32 v64, v108, 1.0, v64 op_sel_hi:[1,0,0]
	v_fma_mix_f32 v65, v108, 1.0, v65 op_sel:[1,0,0] op_sel_hi:[1,0,0]
	v_fma_mix_f32 v68, v112, 1.0, v68 op_sel_hi:[1,0,0]
	v_fma_mix_f32 v69, v112, 1.0, v69 op_sel:[1,0,0] op_sel_hi:[1,0,0]
	v_fma_mix_f32 v62, v109, 1.0, v62 op_sel_hi:[1,0,0]
	v_fma_mix_f32 v63, v109, 1.0, v63 op_sel:[1,0,0] op_sel_hi:[1,0,0]
	v_fma_mix_f32 v66, v113, 1.0, v66 op_sel_hi:[1,0,0]
	v_fma_mix_f32 v67, v113, 1.0, v67 op_sel:[1,0,0] op_sel_hi:[1,0,0]
	s_mov_b64 exec, -1
	s_waitcnt vmcnt(0)
	s_cmp_eq_u64 s[4:5], 0
	s_cbranch_scc0 .Lnowp_a0
	v_readfirstlane_b32 s60, v0
	v_and_b32_e32 v79, 63, v0
	s_nop 3
	s_lshr_b32 s60, s60, 6
	s_mul_i32 s60, s60, 0x6800
	s_add_u32 s62, s34, s60
	s_addc_u32 s63, s35, 0
	v_lshlrev_b32_e32 v79, 4, v79
	global_load_dwordx4 v[88:91], v79, s[62:63]
	global_load_dwordx4 v[106:109], v79, s[62:63] offset:1024
	global_load_dwordx4 v[110:113], v79, s[62:63] offset:2048
	global_load_dwordx4 v[114:117], v79, s[62:63] offset:3072

.LBB3_10:
	s_or_b64 exec, exec, s[10:11]
	v_mov_b32_e32 v52, 0x7bff7bff
	v_mov_b32_e32 v99, 0x7bff7bff
	v_mov_b32_e32 v98, 0x7bff7bff
	v_mov_b32_e32 v103, 0x7bff7bff
	v_mov_b32_e32 v100, 0xfbfffbff
	v_mov_b32_e32 v101, 0xfbfffbff
	v_mov_b32_e32 v105, 0xfbfffbff
	v_mov_b32_e32 v104, 0xfbfffbff
	v_mov_b64_e32 v[62:63], 0
	v_mov_b64_e32 v[64:65], 0
	v_mov_b64_e32 v[66:67], 0
	v_mov_b64_e32 v[68:69], 0
	v_mov_b64_e32 v[70:71], 0
	v_mov_b64_e32 v[72:73], 0
	v_mov_b64_e32 v[74:75], 0
	v_mov_b64_e32 v[76:77], 0
	v_cmp_lt_i32_e64 s[10:11], v50, v97
	v_mov_b32_e32 v91, v97
	v_and_b32_e32 v92, 3, v50
	s_waitcnt lgkmcnt(0)
	v_cndmask_b32_e64 v10, v11, v10, s[10:11]
	v_add_u32_e32 v92, 8, v92
	v_add_u32_e32 v93, -1, v97
	v_cndmask_b32_e64 v81, 0, v10, s[0:1]
	v_cndmask_b32_e64 v93, 0, v93, s[0:1]
	v_cndmask_b32_e64 v94, 0, v78, s[0:1]
	v_lshlrev_b32_e32 v81, 7, v81
	v_min_i32_e32 v116, v92, v93
	v_add_u32_e32 v117, 4, v92
	v_min_i32_e32 v117, v117, v93
	v_add_lshl_u32 v116, v116, v94, 2
	v_add_lshl_u32 v117, v117, v94, 2
	global_load_dword v87, v116, s[20:21]
	global_load_dword v88, v117, s[20:21]
	v_add_u32_e32 v92, 8, v92
	v_mov_b32_e32 v89, v81
	v_mov_b32_e32 v90, v81
	s_nop 1
	v_mov_b32_dpp v89, v81 row_shr:4 row_mask:0xf bank_mask:0xa
	v_mov_b32_dpp v90, v81 row_shl:4 row_mask:0xf bank_mask:0x5
	s_mov_b64 s[78:79], 0xff
	v_cmp_gt_i32_e64 s[44:45], v91, 0
	v_cmp_gt_i32_e64 s[46:47], v91, 1
	v_cmp_gt_i32_e64 s[48:49], v91, 2
	v_cmp_gt_i32_e64 s[50:51], v91, 3
	v_cmp_gt_i32_e64 s[52:53], v91, 4
	v_cmp_gt_i32_e64 s[54:55], v91, 5
	v_cmp_gt_i32_e64 s[56:57], v91, 6
	v_cmp_gt_i32_e64 s[58:59], v91, 7
	s_nop 0
	v_or_b32_dpp v79, v89, v56 quad_perm:[0,0,0,0] row_mask:0xf bank_mask:0xf
	v_or_b32_dpp v80, v89, v56 quad_perm:[1,1,1,1] row_mask:0xf bank_mask:0xf
	s_or_b64 exec, s[44:45], s[78:79]
	global_load_dwordx4 v[10:13], v79, s[24:25]
	global_load_dwordx4 v[14:17], v80, s[24:25]
	s_mov_b64 exec, -1
	s_nop 0
	v_or_b32_dpp v79, v89, v56 quad_perm:[2,2,2,2] row_mask:0xf bank_mask:0xf
	v_or_b32_dpp v80, v89, v56 quad_perm:[3,3,3,3] row_mask:0xf bank_mask:0xf
	s_or_b64 exec, s[48:49], s[78:79]
	global_load_dwordx4 v[18:21], v79, s[24:25]
	global_load_dwordx4 v[22:25], v80, s[24:25]
	s_mov_b64 exec, -1
	s_nop 0
	v_or_b32_dpp v79, v90, v56 quad_perm:[0,0,0,0] row_mask:0xf bank_mask:0xf
	v_or_b32_dpp v80, v90, v56 quad_perm:[1,1,1,1] row_mask:0xf bank_mask:0xf
	s_or_b64 exec, s[52:53], s[78:79]
	global_load_dwordx4 v[26:29], v79, s[24:25]
	global_load_dwordx4 v[30:33], v80, s[24:25]
	s_mov_b64 exec, -1
	s_nop 0
	v_or_b32_dpp v79, v90, v56 quad_perm:[2,2,2,2] row_mask:0xf bank_mask:0xf
	v_or_b32_dpp v80, v90, v56 quad_perm:[3,3,3,3] row_mask:0xf bank_mask:0xf
	s_or_b64 exec, s[56:57], s[78:79]
	global_load_dwordx4 v[34:37], v79, s[24:25]
	global_load_dwordx4 v[38:41], v80, s[24:25]
	s_mov_b64 exec, -1
	v_cmp_gt_i32_e64 s[60:61], v91, 8
	s_cmp_lg_u64 s[60:61], 0
	s_cbranch_scc0 .Lpl_last_a1
.Lpl_steady_a1:
	s_waitcnt vmcnt(6)
	v_lshlrev_b32_e32 v89, 7, v87
	v_lshlrev_b32_e32 v90, 7, v88
	v_min_i32_e32 v116, v92, v93
	v_add_u32_e32 v117, 4, v92
	v_min_i32_e32 v117, v117, v93
	v_add_lshl_u32 v116, v116, v94, 2
	v_add_lshl_u32 v117, v117, v94, 2
	global_load_dword v87, v116, s[20:21]
	global_load_dword v88, v117, s[20:21]
	v_add_u32_e32 v92, 8, v92
	v_cmp_gt_i32_e64 s[62:63], v91, 8
	v_cmp_gt_i32_e64 s[64:65], v91, 9
	v_cmp_gt_i32_e64 s[66:67], v91, 10
	v_cmp_gt_i32_e64 s[68:69], v91, 11
	v_cmp_gt_i32_e64 s[70:71], v91, 12
	v_cmp_gt_i32_e64 s[72:73], v91, 13
	v_cmp_gt_i32_e64 s[74:75], v91, 14
	v_cmp_gt_i32_e64 s[76:77], v91, 15
	s_mov_b64 exec, s[44:45]
	v_pk_minimum3_f16 v52, v52, v10, v14
	v_pk_maximum3_f16 v100, v100, v10, v14
	v_pk_minimum3_f16 v99, v99, v11, v15
	v_pk_maximum3_f16 v101, v101, v11, v15
	v_pk_minimum3_f16 v98, v98, v12, v16
	v_pk_maximum3_f16 v105, v105, v12, v16
	v_pk_minimum3_f16 v103, v103, v13, v17
	v_pk_maximum3_f16 v104, v104, v13, v17
	v_pk_mul_f16 v110, v10, v10
	v_mov_b32_e32 v106, v10
	v_pk_mul_f16 v111, v11, v11
	v_mov_b32_e32 v107, v11
	v_pk_mul_f16 v112, v12, v12
	v_mov_b32_e32 v108, v12
	v_pk_mul_f16 v113, v13, v13
	v_mov_b32_e32 v109, v13
	s_mov_b64 exec, s[46:47]
	v_pk_add_f16 v106, v106, v14
	v_pk_fma_f16 v110, v14, v14, v110
	v_pk_add_f16 v107, v107, v15
	v_pk_fma_f16 v111, v15, v15, v111
	v_pk_add_f16 v108, v108, v16
	v_pk_fma_f16 v112, v16, v16, v112
	v_pk_add_f16 v109, v109, v17
	v_pk_fma_f16 v113, v17, v17, v113
	s_mov_b64 exec, -1
	s_nop 0
	v_or_b32_dpp v79, v89, v56 quad_perm:[0,0,0,0] row_mask:0xf bank_mask:0xf
	v_or_b32_dpp v80, v89, v56 quad_perm:[1,1,1,1] row_mask:0xf bank_mask:0xf
	s_or_b64 exec, s[62:63], s[78:79]
	global_load_dwordx4 v[10:13], v79, s[24:25]
	global_load_dwordx4 v[14:17], v80, s[24:25]
	s_mov_b64 exec, -1
	s_waitcnt vmcnt(8)
	s_mov_b64 exec, s[48:49]
	v_pk_minimum3_f16 v52, v52, v18, v22
	v_pk_maximum3_f16 v100, v100, v18, v22
	v_pk_minimum3_f16 v99, v99, v19, v23
	v_pk_maximum3_f16 v101, v101, v19, v23
	v_pk_minimum3_f16 v98, v98, v20, v24
	v_pk_maximum3_f16 v105, v105, v20, v24
	v_pk_minimum3_f16 v103, v103, v21, v25
	v_pk_maximum3_f16 v104, v104, v21, v25
	v_pk_add_f16 v106, v106, v18
	v_pk_fma_f16 v110, v18, v18, v110
	v_pk_add_f16 v107, v107, v19
	v_pk_fma_f16 v111, v19, v19, v111
	v_pk_add_f16 v108, v108, v20
	v_pk_fma_f16 v112, v20, v20, v112
	v_pk_add_f16 v109, v109, v21
	v_pk_fma_f16 v113, v21, v21, v113
	s_mov_b64 exec, s[50:51]
	v_pk_add_f16 v106, v106, v22
	v_pk_fma_f16 v110, v22, v22, v110
	v_pk_add_f16 v107, v107, v23
	v_pk_fma_f16 v111, v23, v23, v111
	v_pk_add_f16 v108, v108, v24
	v_pk_fma_f16 v112, v24, v24, v112
	v_pk_add_f16 v109, v109, v25
	v_pk_fma_f16 v113, v25, v25, v113
	s_mov_b64 exec, -1
	s_nop 0
	v_or_b32_dpp v79, v89, v56 quad_perm:[2,2,2,2] row_mask:0xf bank_mask:0xf
	v_or_b32_dpp v80, v89, v56 quad_perm:[3,3,3,3] row_mask:0xf bank_mask:0xf
	s_or_b64 exec, s[66:67], s[78:79]
	global_load_dwordx4 v[18:21], v79, s[24:25]
	global_load_dwordx4 v[22:25], v80, s[24:25]
	s_mov_b64 exec, -1
	s_waitcnt vmcnt(8)
	s_mov_b64 exec, s[52:53]
	v_pk_minimum3_f16 v52, v52, v26, v30
	v_pk_maximum3_f16 v100, v100, v26, v30
	v_pk_minimum3_f16 v99, v99, v27, v31
	v_pk_maximum3_f16 v101, v101, v27, v31
	v_pk_minimum3_f16 v98, v98, v28, v32
	v_pk_maximum3_f16 v105, v105, v28, v32
	v_pk_minimum3_f16 v103, v103, v29, v33
	v_pk_maximum3_f16 v104, v104, v29, v33
	v_pk_add_f16 v106, v106, v26
	v_pk_fma_f16 v110, v26, v26, v110
	v_pk_add_f16 v107, v107, v27
	v_pk_fma_f16 v111, v27, v27, v111
	v_pk_add_f16 v108, v108, v28
	v_pk_fma_f16 v112, v28, v28, v112
	v_pk_add_f16 v109, v109, v29
	v_pk_fma_f16 v113, v29, v29, v113
	s_mov_b64 exec, s[54:55]
	v_pk_add_f16 v106, v106, v30
	v_pk_fma_f16 v110, v30, v30, v110
	v_pk_add_f16 v107, v107, v31
	v_pk_fma_f16 v111, v31, v31, v111
	v_pk_add_f16 v108, v108, v32
	v_pk_fma_f16 v112, v32, v32, v112
	v_pk_add_f16 v109, v109, v33
	v_pk_fma_f16 v113, v33, v33, v113
	s_mov_b64 exec, -1
	s_nop 0
	v_or_b32_dpp v79, v90, v56 quad_perm:[0,0,0,0] row_mask:0xf bank_mask:0xf
	v_or_b32_dpp v80, v90, v56 quad_perm:[1,1,1,1] row_mask:0xf bank_mask:0xf
	s_or_b64 exec, s[70:71], s[78:79]
	global_load_dwordx4 v[26:29], v79, s[24:25]
	global_load_dwordx4 v[30:33], v80, s[24:25]
	s_mov_b64 exec, -1
	s_waitcnt vmcnt(8)
	s_mov_b64 exec, s[56:57]
	v_pk_minimum3_f16 v52, v52, v34, v38
	v_pk_maximum3_f16 v100, v100, v34, v38
	v_pk_minimum3_f16 v99, v99, v35, v39
	v_pk_maximum3_f16 v101, v101, v35, v39
	v_pk_minimum3_f16 v98, v98, v36, v40
	v_pk_maximum3_f16 v105, v105, v36, v40
	v_pk_minimum3_f16 v103, v103, v37, v41
	v_pk_maximum3_f16 v104, v104, v37, v41
	v_pk_add_f16 v106, v106, v34
	v_pk_fma_f16 v110, v34, v34, v110
	v_pk_add_f16 v107, v107, v35
	v_pk_fma_f16 v111, v35, v35, v111
	v_pk_add_f16 v108, v108, v36
	v_pk_fma_f16 v112, v36, v36, v112
	v_pk_add_f16 v109, v109, v37
	v_pk_fma_f16 v113, v37, v37, v113
	s_mov_b64 exec, s[58:59]
	v_pk_add_f16 v106, v106, v38
	v_pk_fma_f16 v110, v38, v38, v110
	v_pk_add_f16 v107, v107, v39
	v_pk_fma_f16 v111, v39, v39, v111
	v_pk_add_f16 v108, v108, v40
	v_pk_fma_f16 v112, v40, v40, v112
	v_pk_add_f16 v109, v109, v41
	v_pk_fma_f16 v113, v41, v41, v113
	s_mov_b64 exec, -1
	s_nop 0
	v_or_b32_dpp v79, v90, v56 quad_perm:[2,2,2,2] row_mask:0xf bank_mask:0xf
	v_or_b32_dpp v80, v90, v56 quad_perm:[3,3,3,3] row_mask:0xf bank_mask:0xf
	s_or_b64 exec, s[74:75], s[78:79]
	global_load_dwordx4 v[34:37], v79, s[24:25]
	global_load_dwordx4 v[38:41], v80, s[24:25]
	s_mov_b64 exec, -1
	s_mov_b64 exec, s[44:45]
	v_fma_mix_f32 v72, v106, 1.0, v72 op_sel_hi:[1,0,0]
	v_fma_mix_f32 v73, v106, 1.0, v73 op_sel:[1,0,0] op_sel_hi:[1,0,0]
	v_fma_mix_f32 v76, v110, 1.0, v76 op_sel_hi:[1,0,0]
	v_fma_mix_f32 v77, v110, 1.0, v77 op_sel:[1,0,0] op_sel_hi:[1,0,0]
	v_fma_mix_f32 v70, v107, 1.0, v70 op_sel_hi:[1,0,0]
	v_fma_mix_f32 v71, v107, 1.0, v71 op_sel:[1,0,0] op_sel_hi:[1,0,0]
	v_fma_mix_f32 v74, v111, 1.0, v74 op_sel_hi:[1,0,0]
	v_fma_mix_f32 v75, v111, 1.0, v75 op_sel:[1,0,0] op_sel_hi:[1,0,0]
	v_fma_mix_f32 v64, v108, 1.0, v64 op_sel_hi:[1,0,0]
	v_fma_mix_f32 v65, v108, 1.0, v65 op_sel:[1,0,0] op_sel_hi:[1,0,0]
	v_fma_mix_f32 v68, v112, 1.0, v68 op_sel_hi:[1,0,0]
	v_fma_mix_f32 v69, v112, 1.0, v69 op_sel:[1,0,0] op_sel_hi:[1,0,0]
	v_fma_mix_f32 v62, v109, 1.0, v62 op_sel_hi:[1,0,0]
	v_fma_mix_f32 v63, v109, 1.0, v63 op_sel:[1,0,0] op_sel_hi:[1,0,0]
	v_fma_mix_f32 v66, v113, 1.0, v66 op_sel_hi:[1,0,0]
	v_fma_mix_f32 v67, v113, 1.0, v67 op_sel:[1,0,0] op_sel_hi:[1,0,0]
	s_mov_b64 exec, -1
	s_mov_b64 s[44:45], s[62:63]
	s_mov_b64 s[46:47], s[64:65]
	s_mov_b64 s[48:49], s[66:67]
	s_mov_b64 s[50:51], s[68:69]
	s_mov_b64 s[52:53], s[70:71]
	s_mov_b64 s[54:55], s[72:73]
	s_mov_b64 s[56:57], s[74:75]
	s_mov_b64 s[58:59], s[76:77]
	v_add_u32_e32 v91, -8, v91
	v_cmp_gt_i32_e64 s[60:61], v91, 8
	s_cmp_lg_u64 s[60:61], 0
	s_cbranch_scc1 .Lpl_steady_a1

.Lpl_fold_a1:
	s_mov_b64 exec, s[44:45]
	v_fma_mix_f32 v72, v106, 1.0, v72 op_sel_hi:[1,0,0]
	v_fma_mix_f32 v73, v106, 1.0, v73 op_sel:[1,0,0] op_sel_hi:[1,0,0]
	v_fma_mix_f32 v76, v110, 1.0, v76 op_sel_hi:[1,0,0]
	v_fma_mix_f32 v77, v110, 1.0, v77 op_sel:[1,0,0] op_sel_hi:[1,0,0]
	v_fma_mix_f32 v70, v107, 1.0, v70 op_sel_hi:[1,0,0]
	v_fma_mix_f32 v71, v107, 1.0, v71 op_sel:[1,0,0] op_sel_hi:[1,0,0]
	v_fma_mix_f32 v74, v111, 1.0, v74 op_sel_hi:[1,0,0]
	v_fma_mix_f32 v75, v111, 1.0, v75 op_sel:[1,0,0] op_sel_hi:[1,0,0]
	v_fma_mix_f32 v64, v108, 1.0, v64 op_sel_hi:[1,0,0]
	v_fma_mix_f32 v65, v108, 1.0, v65 op_sel:[1,0,0] op_sel_hi:[1,0,0]
	v_fma_mix_f32 v68, v112, 1.0, v68 op_sel_hi:[1,0,0]
	v_fma_mix_f32 v69, v112, 1.0, v69 op_sel:[1,0,0] op_sel_hi:[1,0,0]
	v_fma_mix_f32 v62, v109, 1.0, v62 op_sel_hi:[1,0,0]
	v_fma_mix_f32 v63, v109, 1.0, v63 op_sel:[1,0,0] op_sel_hi:[1,0,0]
	v_fma_mix_f32 v66, v113, 1.0, v66 op_sel_hi:[1,0,0]
	v_fma_mix_f32 v67, v113, 1.0, v67 op_sel:[1,0,0] op_sel_hi:[1,0,0]
	s_mov_b64 exec, -1
	s_waitcnt vmcnt(0)
	s_cmp_eq_u64 s[4:5], 0
	s_cbranch_scc0 .Lnowp_a1
	v_readfirstlane_b32 s60, v0
	v_and_b32_e32 v79, 63, v0
	s_nop 3
	s_lshr_b32 s60, s60, 6
	s_mul_i32 s60, s60, 0x6800
	s_add_u32 s62, s12, s60
	s_addc_u32 s63, s13, 0
	v_lshlrev_b32_e32 v79, 4, v79
	global_load_dwordx4 v[88:91], v79, s[62:63]
	global_load_dwordx4 v[106:109], v79, s[62:63] offset:1024
	global_load_dwordx4 v[110:113], v79, s[62:63] offset:2048
	global_load_dwordx4 v[114:117], v79, s[62:63] offset:3072
